# LN1 row loop: next row's three HBM loads issued mid-row into spare registers (copied at the top of the next iteration) instead of load-then-wait at the top of every row
# speedup vs baseline: 1.0026x; 1.0026x over previous
; #define GAS __attribute__((address_space(1)))
; __device__ __forceinline__ void unpack8(const u32x4 q, float* o) { o[0] = bflo(q.x); o[1] = bfhi(q.x); o[2] = bflo(q.y); o[3] = bfhi(q.y); o[4] = bflo(q.z); o[5] = bfhi(q.z); o[6] = bflo(q.w); o[7] = bfhi(q.w); }
; __device__ __forceinline__ const float* mod_ptr(const Frame& F, int l, int row) { return (const float*)(F.ws + WS_MOD) + ((size_t)l * 17 + row_b(row)) * 6144; }
; __device__ __forceinline__ void ph_ln1(Frame& F, int l, int ntok) {
;     const int gw = F.wg * NWAVES + F.wave, NGW = F.G * NWAVES;
;     const int cA = 256 * (F.lane >> 4) + 32 * ((F.lane >> 2) & 3) + 8 * (F.lane & 3);
;     ...
;     const float* lg = F.in[I_LN1G] + l * DM; const float* lb = F.in[I_LN1B] + l * DM;
;     for (int row = gw; row < ntok; row += NGW) {
;         bf16_t* xr = (bf16_t*)(F.ws + WS_XR) + (size_t)row * DM;
;         const unsigned char* yr = (const unsigned char*)(F.ws + WS_Y) + (size_t)row * DM + 16 * F.lane;
;         const float* md = mod_ptr(F, l, row);
;         const u32x4 xa = __builtin_nontemporal_load((const GAS u32x4*)(xr + cA)), xb = __builtin_nontemporal_load((const GAS u32x4*)(xr + cA + 128)), ya = __builtin_nontemporal_load((const GAS u32x4*)yr);
;         float x[16], y[16], v[16]; unpack8(xa, x); unpack8(xb, x + 8);
.LBB0_772:
	s_andn2_b64 vcc, exec, s[2:3]
	s_cbranch_vccnz .LBB0_826
	v_readlane_b32 s36, v252, 8
	v_readlane_b32 s37, v252, 9
	s_mov_b32 s0, s97
	v_readlane_b32 s38, v252, 10
	v_readlane_b32 s39, v252, 11
	s_mov_b64 s[2:3], s[36:37]
	v_mbcnt_lo_u32_b32 v0, -1, 0
	v_mbcnt_hi_u32_b32 v0, -1, v0
	v_readlane_b32 s8, v255, 14
	v_readlane_b32 s2, v254, 28
	s_add_i32 s40, s0, s2
	v_readlane_b32 s9, v255, 15
	v_readlane_b32 s10, v255, 3
	v_readlane_b32 s18, v255, 5
	s_cmp_ge_i32 s40, s80
	v_readlane_b32 s11, v255, 4
	v_readlane_b32 s19, v255, 6
	s_mov_b32 s9, 0xf800000
	s_mov_b32 s20, 0x3fd744fd
	s_cbranch_scc1 .LBB0_776
	s_lshl_b32 s22, s30, 10
	v_readlane_b32 s44, v252, 16
	s_lshl_b64 s[2:3], s[22:23], 2
	v_readlane_b32 s46, v252, 18
	v_readlane_b32 s47, v252, 19
	s_add_u32 s4, s46, s2
	s_addc_u32 s5, s47, s3
	v_lshlrev_b32_e32 v1, 3, v0
	v_readlane_b32 s45, v252, 17
	s_add_u32 s2, s44, s2
	v_lshlrev_b32_e32 v2, 4, v0
	v_and_b32_e32 v1, 0x78, v1
	s_movk_i32 s0, 0xff00
	s_addc_u32 s3, s45, s3
	s_waitcnt vmcnt(0)
	v_and_or_b32 v4, v2, s0, v1
	v_ashrrev_i32_e32 v5, 31, v4
	s_add_u32 s22, s38, 0x100000
	v_lshlrev_b64 v[54:55], 2, v[4:5]
	s_addc_u32 s42, s39, 0
	s_ashr_i32 s41, s40, 31
	v_lshl_add_u64 v[56:57], s[2:3], 0, v[54:55]
	v_lshl_add_u64 v[58:59], s[4:5], 0, v[54:55]
	s_lshl_b64 s[2:3], s[40:41], 10
	s_lshl_b64 s[4:5], s[40:41], 11
	v_or_b32_e32 v6, 0x80, v4
	v_lshl_add_u64 v[60:61], s[2:3], 0, v[4:5]
	s_add_u32 s2, s2, 0x52900000
	v_ashrrev_i32_e32 v7, 31, v6
	v_ashrrev_i32_e32 v3, 31, v2
	v_lshlrev_b32_e32 v0, 2, v0
	s_addc_u32 s3, s3, 0
	v_xor_b32_e32 v76, 4, v0
	v_xor_b32_e32 v77, 8, v0
	v_xor_b32_e32 v78, 16, v0
	v_xor_b32_e32 v79, 32, v0
	v_xor_b32_e32 v80, 64, v0
	v_xor_b32_e32 v81, 0x80, v0
	v_lshl_add_u64 v[62:63], v[4:5], 1, s[4:5]
	v_lshl_add_u64 v[64:65], s[2:3], 0, v[2:3]
	v_lshlrev_b64 v[66:67], 2, v[6:7]
	v_readlane_b32 s48, v252, 20
	v_readlane_b32 s49, v252, 21
	v_readlane_b32 s50, v252, 22
	v_readlane_b32 s51, v252, 23
	v_readlane_b32 s52, v252, 24
	v_readlane_b32 s53, v252, 25
	v_readlane_b32 s54, v252, 26
	v_readlane_b32 s55, v252, 27
	v_readlane_b32 s56, v252, 28
	v_readlane_b32 s57, v252, 29
	v_readlane_b32 s58, v252, 30
	v_readlane_b32 s59, v252, 31
	s_brev_b32 s84, 38
	s_mov_b32 s85, 0
	v_lshl_add_u64 v[148:149], s[38:39], 0, v[62:63]
	v_lshl_add_u64 v[148:149], v[148:149], 0, s[84:85]
	v_lshl_add_u64 v[150:151], s[38:39], 0, v[64:65]
	global_load_dwordx4 v[128:131], v[148:149], off nt
	global_load_dwordx4 v[132:135], v[148:149], off offset:256 nt
	global_load_dwordx4 v[144:147], v[150:151], off nt
.LBB0_775:
	s_min_i32 s0, s40, 0x10000
	s_ashr_i32 s0, s0, 12
	s_ashr_i32 s2, s0, 31
	s_mul_i32 s3, s30, 17
	s_add_u32 s0, s0, s3
	s_addc_u32 s2, s2, 0
	s_mulk_i32 s2, 0x6000
	s_mul_hi_u32 s3, s0, 0x6000
	s_add_i32 s3, s3, s2
	v_lshl_add_u64 v[2:3], s[38:39], 0, v[62:63]
	s_brev_b32 s2, 38
	v_add_co_u32_e32 v68, vcc, s2, v2
	v_lshl_add_u64 v[0:1], s[38:39], 0, v[64:65]
	s_nop 0
	v_addc_co_u32_e32 v69, vcc, 0, v3, vcc
	s_nop 0
	s_mulk_i32 s0, 0x6000
	s_add_u32 s0, s22, s0
	s_addc_u32 s4, s42, s3
	s_add_u32 s2, s0, 0x2000
	s_addc_u32 s3, s4, 0
	s_add_u32 s36, s0, 0x3000
	s_addc_u32 s37, s4, 0
	v_lshl_add_u64 v[62:63], v[62:63], 0, s[18:19]
	v_lshl_add_u64 v[64:65], v[64:65], 0, s[10:11]
	s_waitcnt vmcnt(0)
	v_mov_b32_e32 v46, v128
	v_mov_b32_e32 v47, v129
	v_mov_b32_e32 v48, v130
	v_mov_b32_e32 v49, v131
	v_mov_b32_e32 v90, v132
	v_mov_b32_e32 v91, v133
	v_mov_b32_e32 v92, v134
	v_mov_b32_e32 v93, v135
	v_mov_b32_e32 v0, v144
	v_mov_b32_e32 v1, v145
	v_mov_b32_e32 v2, v146
	v_mov_b32_e32 v3, v147
	v_lshlrev_b32_e32 v122, 16, v93
	v_cvt_pk_f32_fp8_e32 v[24:25], v0
	v_cvt_pk_f32_fp8_sdwa v[70:71], v0 src0_sel:WORD_1
	v_cvt_pk_f32_fp8_e32 v[72:73], v1
	v_cvt_pk_f32_fp8_sdwa v[74:75], v1 src0_sel:WORD_1
	v_lshl_add_u64 v[0:1], s[2:3], 0, v[54:55]
	global_load_dwordx4 v[50:53], v[0:1], off
	global_load_dwordx4 v[94:97], v[0:1], off offset:16
	v_lshl_add_u64 v[0:1], s[2:3], 0, v[66:67]
	global_load_dwordx4 v[98:101], v[0:1], off
	global_load_dwordx4 v[102:105], v[0:1], off offset:16
	s_add_u32 s2, s0, 0x4000
	s_addc_u32 s3, s4, 0
	v_lshl_add_u64 v[0:1], s[36:37], 0, v[54:55]
	v_lshl_add_u64 v[4:5], s[2:3], 0, v[54:55]
	v_cvt_pk_f32_fp8_e32 v[114:115], v2
	v_cvt_pk_f32_fp8_sdwa v[116:117], v2 src0_sel:WORD_1
	v_cvt_pk_f32_fp8_e32 v[118:119], v3
	v_cvt_pk_f32_fp8_sdwa v[120:121], v3 src0_sel:WORD_1
	global_load_dwordx4 v[26:29], v[56:57], off offset:16
	global_load_dwordx4 v[106:109], v[56:57], off
	global_load_dwordx4 v[30:33], v[58:59], off offset:16
	global_load_dwordx4 v[110:113], v[58:59], off
	global_load_dwordx4 v[12:15], v[0:1], off offset:16
	global_load_dwordx4 v[42:45], v[0:1], off
	s_nop 0
	global_load_dwordx4 v[0:3], v[4:5], off offset:16
	s_nop 0
	global_load_dwordx4 v[4:7], v[4:5], off
	v_and_b32_e32 v123, 0xffff0000, v93
	v_lshl_add_u64 v[82:83], s[2:3], 0, v[66:67]
	s_waitcnt lgkmcnt(0)
	global_load_dwordx4 v[8:11], v[56:57], off offset:528
	global_load_dwordx4 v[34:37], v[56:57], off offset:512
	global_load_dwordx4 v[16:19], v[58:59], off offset:528
	global_load_dwordx4 v[38:41], v[58:59], off offset:512
	s_mov_b32 s0, 0x5be00000
	s_add_i32 s40, s40, s8
	s_cmp_lt_i32 s40, s80
	s_waitcnt vmcnt(15)
	v_pk_mul_f32 v[52:53], v[70:71], v[52:53]
	v_lshlrev_b32_e32 v70, 16, v46
	v_and_b32_e32 v71, 0xffff0000, v46
	v_pk_mul_f32 v[24:25], v[24:25], v[50:51]
	s_waitcnt vmcnt(12)
; #define GAS __attribute__((address_space(1)))
; __device__ __forceinline__ void ph_ln1(Frame& F, int l, int ntok) {
;     ...
;         for (int j = 0; j < 4; ++j) { const f32x4 g1 = *(const GAS f32x4*)(md + 2048 + LN1_COL(j));
; #pragma unroll
;             for (int e = 0; e < 4; ++e) { v[4 * j + e] = x[4 * j + e] * DN_ALPHA + g1[e] * y[4 * j + e]; s += v[4 * j + e]; } }
;         const float mean = wave_sum(s, F.lane) * (1.f / DM); float s2 = 0.f;
; #pragma unroll
;         for (int e = 0; e < 16; ++e) { v[e] -= mean; s2 += v[e] * v[e]; }
;         const float rstd = 1.f / sqrtf(wave_sum(s2, F.lane) * (1.f / DM) + LN_EPS);
	v_pk_mul_f32 v[104:105], v[120:121], v[104:105]
	v_lshlrev_b32_e32 v120, 16, v92
	v_and_b32_e32 v121, 0xffff0000, v92
	v_pk_mul_f32 v[92:93], v[118:119], v[102:103]
	v_lshlrev_b32_e32 v102, 16, v91
	v_and_b32_e32 v103, 0xffff0000, v91
	v_pk_mul_f32 v[100:101], v[116:117], v[100:101]
	v_pk_fma_f32 v[24:25], v[70:71], s[20:21], v[24:25] op_sel_hi:[1,0,1]
	v_pk_fma_f32 v[100:101], v[102:103], s[20:21], v[100:101] op_sel_hi:[1,0,1]
	v_lshlrev_b32_e32 v102, 16, v90
	v_and_b32_e32 v103, 0xffff0000, v90
	v_pk_mul_f32 v[90:91], v[114:115], v[98:99]
	v_lshlrev_b32_e32 v98, 16, v49
	v_and_b32_e32 v99, 0xffff0000, v49
	v_pk_mul_f32 v[74:75], v[74:75], v[96:97]
	v_lshlrev_b32_e32 v96, 16, v48
	v_and_b32_e32 v97, 0xffff0000, v48
	v_pk_mul_f32 v[48:49], v[72:73], v[94:95]
	v_lshlrev_b32_e32 v72, 16, v47
	v_and_b32_e32 v73, 0xffff0000, v47
	v_add_f32_e32 v46, 0, v24
	v_pk_fma_f32 v[52:53], v[72:73], s[20:21], v[52:53] op_sel_hi:[1,0,1]
	v_add_f32_e32 v46, v25, v46
	v_add_f32_e32 v46, v52, v46
	v_pk_fma_f32 v[48:49], v[96:97], s[20:21], v[48:49] op_sel_hi:[1,0,1]
	v_add_f32_e32 v46, v53, v46
	v_add_f32_e32 v46, v48, v46
	v_pk_fma_f32 v[74:75], v[98:99], s[20:21], v[74:75] op_sel_hi:[1,0,1]
	v_add_f32_e32 v46, v49, v46
	v_add_f32_e32 v46, v74, v46
	v_pk_fma_f32 v[90:91], v[102:103], s[20:21], v[90:91] op_sel_hi:[1,0,1]
	v_add_f32_e32 v46, v75, v46
	v_add_f32_e32 v46, v90, v46
	v_add_f32_e32 v46, v91, v46
	v_add_f32_e32 v46, v100, v46
	v_pk_fma_f32 v[92:93], v[120:121], s[20:21], v[92:93] op_sel_hi:[1,0,1]
	v_add_f32_e32 v46, v101, v46
	v_add_f32_e32 v46, v92, v46
	v_pk_fma_f32 v[104:105], v[122:123], s[20:21], v[104:105] op_sel_hi:[1,0,1]
	v_add_f32_e32 v46, v93, v46
	v_add_f32_e32 v46, v104, v46
	v_add_f32_e32 v46, v105, v46
	ds_bpermute_b32 v47, v76, v46
	s_waitcnt vmcnt(4)
	v_add_f32_e32 v124, 1.0, v4
	v_add_f32_e32 v125, 1.0, v5
	v_lshl_add_u64 v[4:5], s[36:37], 0, v[66:67]
	v_add_f32_e32 v126, 1.0, v6
	s_waitcnt lgkmcnt(0)
	v_add_f32_e32 v46, v46, v47
	ds_bpermute_b32 v47, v77, v46
	v_add_f32_e32 v127, 1.0, v7
	v_add_f32_e32 v86, 1.0, v0
	v_add_f32_e32 v87, 1.0, v1
	v_add_f32_e32 v88, 1.0, v2
	s_waitcnt lgkmcnt(0)
	v_add_f32_e32 v46, v46, v47
	ds_bpermute_b32 v47, v78, v46
	v_add_f32_e32 v89, 1.0, v3
	global_load_dwordx4 v[0:3], v[4:5], off offset:16
	global_load_dwordx4 v[20:23], v[4:5], off
	s_nop 0
	global_load_dwordx4 v[4:7], v[82:83], off offset:16
	s_nop 0
	global_load_dwordx4 v[82:85], v[82:83], off
	s_cselect_b64 s[86:87], -1, 0
	v_lshl_add_u64 v[148:149], s[38:39], 0, v[62:63]
	v_lshl_add_u64 v[148:149], v[148:149], 0, s[84:85]
	v_lshl_add_u64 v[150:151], s[38:39], 0, v[64:65]
	v_cndmask_b32_e64 v148, v68, v148, s[86:87]
	v_cndmask_b32_e64 v149, v69, v149, s[86:87]
	v_cndmask_b32_e64 v150, v68, v150, s[86:87]
	v_cndmask_b32_e64 v151, v69, v151, s[86:87]
	global_load_dwordx4 v[128:131], v[148:149], off nt
	global_load_dwordx4 v[132:135], v[148:149], off offset:256 nt
	global_load_dwordx4 v[144:147], v[150:151], off nt
	s_waitcnt lgkmcnt(0)
	v_add_f32_e32 v46, v46, v47
	ds_bpermute_b32 v47, v79, v46
	s_waitcnt lgkmcnt(0)
	v_add_f32_e32 v46, v46, v47
	ds_bpermute_b32 v47, v80, v46
	s_waitcnt lgkmcnt(0)
	v_add_f32_e32 v46, v46, v47
	ds_bpermute_b32 v47, v81, v46
	s_waitcnt lgkmcnt(0)
	v_add_f32_e32 v46, v46, v47
	v_mul_f32_e32 v50, 0x3a800000, v46
	v_pk_add_f32 v[24:25], v[24:25], v[50:51] op_sel_hi:[1,0] neg_lo:[0,1] neg_hi:[0,1]
	v_pk_add_f32 v[96:97], v[52:53], v[50:51] op_sel_hi:[1,0] neg_lo:[0,1] neg_hi:[0,1]
	v_pk_mul_f32 v[94:95], v[24:25], v[24:25]
	v_pk_mul_f32 v[98:99], v[96:97], v[96:97]
	v_add_f32_e32 v94, v94, v95
	v_pk_add_f32 v[72:73], v[48:49], v[50:51] op_sel_hi:[1,0] neg_lo:[0,1] neg_hi:[0,1]
	v_add_f32_e32 v94, v98, v94
	v_pk_mul_f32 v[102:103], v[72:73], v[72:73]
	v_add_f32_e32 v94, v99, v94
	v_pk_add_f32 v[74:75], v[74:75], v[50:51] op_sel_hi:[1,0] neg_lo:[0,1] neg_hi:[0,1]
	v_add_f32_e32 v94, v102, v94
	v_pk_mul_f32 v[114:115], v[74:75], v[74:75]
	v_add_f32_e32 v94, v103, v94
	v_pk_add_f32 v[52:53], v[90:91], v[50:51] op_sel_hi:[1,0] neg_lo:[0,1] neg_hi:[0,1]
	v_add_f32_e32 v94, v114, v94
	v_pk_mul_f32 v[90:91], v[52:53], v[52:53]
	v_add_f32_e32 v94, v115, v94
	v_pk_add_f32 v[70:71], v[100:101], v[50:51] op_sel_hi:[1,0] neg_lo:[0,1] neg_hi:[0,1]
	v_add_f32_e32 v90, v90, v94
	v_pk_mul_f32 v[100:101], v[70:71], v[70:71]
	v_add_f32_e32 v90, v91, v90
	v_pk_add_f32 v[46:47], v[92:93], v[50:51] op_sel_hi:[1,0] neg_lo:[0,1] neg_hi:[0,1]
	v_add_f32_e32 v90, v100, v90
	v_pk_mul_f32 v[92:93], v[46:47], v[46:47]
	v_add_f32_e32 v90, v101, v90
	v_pk_add_f32 v[48:49], v[104:105], v[50:51] op_sel_hi:[1,0] neg_lo:[0,1] neg_hi:[0,1]
	v_add_f32_e32 v90, v92, v90
	v_pk_mul_f32 v[50:51], v[48:49], v[48:49]
	v_add_f32_e32 v90, v93, v90
	v_add_f32_e32 v50, v50, v90
	v_add_f32_e32 v50, v51, v50
	ds_bpermute_b32 v51, v76, v50
	s_waitcnt lgkmcnt(0)
; #define GAS __attribute__((address_space(1)))
; __device__ __forceinline__ unsigned pk2(float lo, float hi) { const f32x2 v = {lo, hi}; const bf16v2 b = __builtin_convertvector(v, bf16v2); return __builtin_bit_cast(unsigned, b); }
; __device__ __forceinline__ void ph_ln1(Frame& F, int l, int ntok) {
;     ...
;         const float mean = wave_sum(s, F.lane) * (1.f / DM); float s2 = 0.f;
; #pragma unroll
;         for (int e = 0; e < 16; ++e) { v[e] -= mean; s2 += v[e] * v[e]; }
;         const float rstd = 1.f / sqrtf(wave_sum(s2, F.lane) * (1.f / DM) + LN_EPS);
;         unsigned wx[8]; int w8[4];
; #pragma unroll
;         for (int j = 0; j < 4; ++j) { const f32x4 g = *(const GAS f32x4*)(lg + LN1_COL(j)), bb = *(const GAS f32x4*)(lb + LN1_COL(j)), sh = *(const GAS f32x4*)(md + 3072 + LN1_COL(j)), sc = *(const GAS f32x4*)(md + 4096 + LN1_COL(j));
;             float xn[4];
; #pragma unroll
;             for (int e = 0; e < 4; ++e) xn[e] = v[4 * j + e] * rstd * g[e] + bb[e];
;             wx[2 * j] = pk2(xn[0], xn[1]); wx[2 * j + 1] = pk2(xn[2], xn[3]);
;             const float h0 = xn[0] * (1.f + sc[0]) + sh[0], h1 = xn[1] * (1.f + sc[1]) + sh[1], h2 = xn[2] * (1.f + sc[2]) + sh[2], h3 = xn[3] * (1.f + sc[3]) + sh[3];
;             int v = 0; v = __builtin_amdgcn_cvt_pk_fp8_f32(h0, h1, v, false); v = __builtin_amdgcn_cvt_pk_fp8_f32(h2, h3, v, true); w8[j] = v; }
;         unsigned char* x8 = (unsigned char*)(F.ws + WS_XM8) + (size_t)row * DM;
;         __builtin_nontemporal_store((u32x2){(unsigned)w8[0], (unsigned)w8[1]}, (GAS u32x2*)(x8 + cA)); __builtin_nontemporal_store((u32x2){(unsigned)w8[2], (unsigned)w8[3]}, (GAS u32x2*)(x8 + cA + 128));
;         __builtin_nontemporal_store((u32x4){wx[0], wx[1], wx[2], wx[3]}, (GAS u32x4*)(xr + cA)); __builtin_nontemporal_store((u32x4){wx[4], wx[5], wx[6], wx[7]}, (GAS u32x4*)(xr + cA + 128));
	v_add_f32_e32 v50, v50, v51
	ds_bpermute_b32 v51, v77, v50
	s_waitcnt lgkmcnt(0)
	v_add_f32_e32 v50, v50, v51
	ds_bpermute_b32 v51, v78, v50
	s_waitcnt lgkmcnt(0)
	v_add_f32_e32 v50, v50, v51
	ds_bpermute_b32 v51, v79, v50
	s_waitcnt lgkmcnt(0)
	v_add_f32_e32 v50, v50, v51
	ds_bpermute_b32 v51, v80, v50
	s_waitcnt vmcnt(4)
	v_add_f32_e32 v4, 1.0, v4
	s_waitcnt vmcnt(3)
	v_add_f32_e32 v82, 1.0, v82
	v_add_f32_e32 v83, 1.0, v83
	s_waitcnt lgkmcnt(0)
	v_add_f32_e32 v50, v50, v51
	ds_bpermute_b32 v51, v81, v50
	v_add_f32_e32 v84, 1.0, v84
	v_add_f32_e32 v85, 1.0, v85
	s_waitcnt lgkmcnt(0)
	v_add_f32_e32 v50, v50, v51
	v_fmamk_f32 v50, v50, 0x3a800000, v234
	v_cmp_gt_f32_e32 vcc, s9, v50
	v_mul_f32_e32 v51, 0x4f800000, v50
	s_nop 0
	v_cndmask_b32_e32 v50, v50, v51, vcc
	v_sqrt_f32_e32 v51, v50
	s_nop 0
	v_add_u32_e32 v90, -1, v51
	v_fma_f32 v91, -v90, v51, v50
	v_cmp_ge_f32_e64 s[36:37], 0, v91
	v_add_u32_e32 v91, 1, v51
	s_nop 0
	v_cndmask_b32_e64 v90, v51, v90, s[36:37]
	v_fma_f32 v51, -v91, v51, v50
	v_cmp_lt_f32_e64 s[36:37], 0, v51
	s_nop 1
	v_cndmask_b32_e64 v51, v90, v91, s[36:37]
	v_mul_f32_e32 v90, 0x37800000, v51
	v_cndmask_b32_e32 v51, v51, v90, vcc
	v_cmp_class_f32_e32 vcc, v50, v232
	s_nop 1
	v_cndmask_b32_e32 v50, v51, v50, vcc
	v_div_scale_f32 v51, s[2:3], v50, v50, 1.0
	v_rcp_f32_e32 v90, v51
	s_nop 0
	v_fma_f32 v91, -v51, v90, 1.0
	v_fmac_f32_e32 v90, v91, v90
	v_div_scale_f32 v91, vcc, 1.0, v50, 1.0
	v_mul_f32_e32 v92, v91, v90
	v_fma_f32 v93, -v51, v92, v91
	v_fmac_f32_e32 v92, v93, v90
	v_fma_f32 v51, -v51, v92, v91
	v_div_fmas_f32 v51, v51, v90, v92
	v_div_fixup_f32 v50, v51, v50, 1.0
	v_pk_mul_f32 v[24:25], v[24:25], v[50:51] op_sel_hi:[1,0]
	s_nop 0
	v_pk_fma_f32 v[90:91], v[106:107], v[24:25], v[110:111]
	v_pk_mul_f32 v[24:25], v[96:97], v[50:51] op_sel_hi:[1,0]
	v_fma_f32 v42, v124, v90, v42
	v_pk_fma_f32 v[92:93], v[108:109], v[24:25], v[112:113]
	v_cvt_pk_bf16_f32 v24, v90, v91
	v_fma_f32 v43, v125, v91, v43
	v_mov_b32_e32 v90, v193
	v_cvt_pk_fp8_f32 v90, v42, v43
	v_pk_mul_f32 v[42:43], v[72:73], v[50:51] op_sel_hi:[1,0]
	v_mov_b32_e32 v91, v193
	v_pk_fma_f32 v[30:31], v[26:27], v[42:43], v[30:31]
	v_pk_mul_f32 v[26:27], v[74:75], v[50:51] op_sel_hi:[1,0]
	v_fma_f32 v12, v86, v30, v12
	v_fma_f32 v13, v87, v31, v13
	v_cvt_pk_fp8_f32 v91, v12, v13
	v_pk_fma_f32 v[28:29], v[28:29], v[26:27], v[32:33]
	v_pk_mul_f32 v[12:13], v[52:53], v[50:51] op_sel_hi:[1,0]
	v_fma_f32 v14, v88, v28, v14
	v_fmac_f32_e32 v15, v89, v29
	v_cvt_pk_fp8_f32 v91, v14, v15 op_sel:[0,0,1]
	v_pk_fma_f32 v[14:15], v[34:35], v[12:13], v[38:39]
	v_pk_mul_f32 v[12:13], v[70:71], v[50:51] op_sel_hi:[1,0]
	v_cvt_pk_bf16_f32 v27, v28, v29
	v_pk_fma_f32 v[28:29], v[36:37], v[12:13], v[40:41]
	v_cvt_pk_bf16_f32 v12, v14, v15
	v_fma_f32 v14, v82, v14, v20
	v_fma_f32 v15, v83, v15, v21
	v_mov_b32_e32 v20, v193
	v_cvt_pk_fp8_f32 v20, v14, v15
	v_pk_mul_f32 v[14:15], v[46:47], v[50:51] op_sel_hi:[1,0]
	v_fma_f32 v21, v84, v28, v22
	v_pk_fma_f32 v[8:9], v[8:9], v[14:15], v[16:17]
	v_fmac_f32_e32 v23, v85, v29
	v_fma_f32 v0, v4, v8, v0
	v_add_f32_e32 v4, 1.0, v5
	v_cvt_pk_fp8_f32 v20, v21, v23 op_sel:[0,0,1]
	v_fma_f32 v1, v4, v9, v1
	v_mov_b32_e32 v21, v193
	v_pk_mul_f32 v[14:15], v[48:49], v[50:51] op_sel_hi:[1,0]
	v_cvt_pk_fp8_f32 v21, v0, v1
	v_pk_fma_f32 v[10:11], v[10:11], v[14:15], v[18:19]
	v_add_f32_e32 v4, 1.0, v6
	v_fma_f32 v44, v126, v92, v44
	v_fmac_f32_e32 v45, v127, v93
	v_fma_f32 v2, v4, v10, v2
	v_add_f32_e32 v4, 1.0, v7
	v_cvt_pk_fp8_f32 v90, v44, v45 op_sel:[0,0,1]
	v_fmac_f32_e32 v3, v4, v11
	v_cvt_pk_fp8_f32 v21, v2, v3 op_sel:[0,0,1]
	v_lshl_add_u64 v[0:1], s[38:39], 0, v[60:61]
	v_add_co_u32_e32 v0, vcc, s0, v0
	v_lshl_add_u64 v[60:61], v[60:61], 0, s[10:11]
	s_nop 0
	v_addc_co_u32_e32 v1, vcc, 0, v1, vcc
	v_cvt_pk_bf16_f32 v25, v92, v93
	v_cvt_pk_bf16_f32 v26, v30, v31
	v_cvt_pk_bf16_f32 v13, v28, v29
	v_cvt_pk_bf16_f32 v14, v8, v9
	v_cvt_pk_bf16_f32 v15, v10, v11
	global_store_dwordx2 v[0:1], v[90:91], off nt
	global_store_dwordx2 v[0:1], v[20:21], off offset:128 nt
	global_store_dwordx4 v[68:69], v[24:27], off nt
	global_store_dwordx4 v[68:69], v[12:15], off offset:256 nt
	s_cbranch_scc1 .LBB0_775
